# code placement: only the code after the L1 attention region shifted +8 bytes (attention loops as in v042)
# baseline (speedup 1.0000x reference)
.LBB0_959:
	v_max_f32_e32 v16, v16, v16
	v_max_f32_e32 v17, 0, v16
	v_exp_f32_e64 v16, -v17
	v_cmp_gt_u32_e32 vcc, 32, v230
	s_and_saveexec_b64 s[2:3], vcc
	ds_write_b32 v235, v16
	s_or_b64 exec, exec, s[2:3]
	v_sub_f32_e32 v113, v113, v17
	v_sub_f32_e32 v112, v112, v17
	v_sub_f32_e32 v111, v111, v17
	v_sub_f32_e32 v110, v110, v17
	v_sub_f32_e32 v109, v109, v17
	v_sub_f32_e32 v108, v108, v17
	v_sub_f32_e32 v107, v107, v17
	v_sub_f32_e32 v106, v106, v17
	v_sub_f32_e32 v105, v105, v17
	v_sub_f32_e32 v104, v104, v17
	v_sub_f32_e32 v103, v103, v17
	v_sub_f32_e32 v102, v102, v17
	v_sub_f32_e32 v101, v101, v17
	v_sub_f32_e32 v100, v100, v17
	v_sub_f32_e32 v99, v99, v17
	v_sub_f32_e32 v98, v98, v17
	v_sub_f32_e32 v97, v97, v17
	v_sub_f32_e32 v96, v96, v17
	v_sub_f32_e32 v95, v95, v17
	v_sub_f32_e32 v94, v94, v17
	v_sub_f32_e32 v93, v93, v17
	v_sub_f32_e32 v92, v92, v17
	v_sub_f32_e32 v91, v91, v17
	v_sub_f32_e32 v90, v90, v17
	v_sub_f32_e32 v89, v89, v17
	v_sub_f32_e32 v88, v88, v17
	v_sub_f32_e32 v87, v87, v17
	v_sub_f32_e32 v86, v86, v17
	v_sub_f32_e32 v85, v85, v17
	v_sub_f32_e32 v84, v84, v17
	v_sub_f32_e32 v83, v83, v17
	v_sub_f32_e32 v82, v82, v17
	v_mul_f32_e32 v243, v243, v16
	s_branch .LBB0_953
	s_nop 0
	s_nop 0
.LBB0_962:
	v_mov_b32_e32 v52, v0
	s_barrier
	s_ashr_i32 s21, s20, 31
	v_readfirstlane_b32 s0, v52
	s_ashr_i32 s2, s0, 2
	s_and_b32 s29, s2, -16
	s_ashr_i32 s3, s0, 7
	v_lshlrev_b32_e32 v2, 4, v52
	v_and_b32_e32 v38, 48, v52
	v_mov_b32_e32 v39, 0
	v_and_b32_e32 v59, 48, v2
	v_lshl_add_u64 v[2:3], s[14:15], 0, v[38:39]
	s_mov_b64 s[0:1], 0x120000
	s_cmp_gt_i32 s3, -1
	v_lshl_add_u64 v[42:43], v[2:3], 0, s[0:1]
	s_cselect_b64 s[0:1], -1, 0
	s_cmp_gt_i32 s3, 0
	v_ashrrev_i32_e32 v58, 2, v52
	s_cselect_b64 s[16:17], -1, 0
	s_cmp_gt_i32 s3, 1
	s_movk_i32 s4, 0x1200
	v_and_b32_e32 v1, 63, v52
	s_cselect_b64 s[18:19], -1, 0
	s_cmp_gt_i32 s3, 2
	v_bfi_b32 v44, -16, s2, v52
	v_mad_i64_i32 v[2:3], s[2:3], v58, s4, 0
	v_mov_b32_e32 v8, 0x90000
	v_lshlrev_b32_e32 v1, 2, v1
	v_mad_i64_i32 v[2:3], s[2:3], s20, v8, v[2:3]
	v_xor_b32_e32 v45, 4, v1
	v_xor_b32_e32 v53, 8, v1
	s_cselect_b64 s[22:23], -1, 0
	v_and_b32_e32 v1, 3, v52
	s_add_u32 s2, s94, s46
	v_lshl_or_b32 v2, v1, 5, v2
	s_addc_u32 s3, s95, 0
	v_bfe_u32 v41, v52, 4, 2
	v_lshl_add_u64 v[46:47], s[2:3], 0, v[2:3]
	v_mad_i64_i32 v[2:3], s[4:5], v44, s4, 0
	v_lshlrev_b32_e32 v40, 3, v41
	v_mad_i64_i32 v[2:3], s[4:5], s20, v8, v[2:3]
	v_or_b32_e32 v2, v2, v40
	v_and_b32_e32 v55, 15, v52
	v_lshl_add_u64 v[2:3], s[2:3], 0, v[2:3]
	s_mov_b64 s[2:3], 0x10a00040
	v_lshl_add_u32 v4, v58, 1, 0
	v_add_u32_e32 v5, 0, v38
	v_mul_u32_u24_e32 v6, 0x110, v59
	v_mul_u32_u24_e32 v7, 0x110, v55
	v_lshl_add_u64 v[48:49], v[2:3], 0, s[2:3]
	v_cndmask_b32_e64 v2, 0, 1, s[0:1]
	s_mov_b64 s[24:25], 0
	s_mov_b64 s[26:27], 0x10a00200
	v_mov_b32_e32 v39, 0x3727c5ac
	s_mov_b32 s28, 0xf800000
	v_mov_b32_e32 v54, 0x260
	s_movk_i32 s30, 0x7fff
	v_add_u32_e32 v56, v4, v6
	v_cmp_ne_u32_e64 s[2:3], 1, v2
	v_add_u32_e32 v57, v5, v7
	v_mov_b32_e32 v60, 1
	v_readlane_b32 s51, v254, 39
	s_branch .LBB0_964
